# Z_nt
# baseline (speedup 1.0000x reference)
.Ljoin:
	s_waitcnt vmcnt(3)
	ds_write_b128 v2, v[8:11]
	ds_write_b128 v2, v[12:15] offset:1024
	ds_write_b128 v2, v[16:19] offset:2048
	s_waitcnt lgkmcnt(0)
	s_barrier
	v_mov_b32_e32 v6, 0x3000
	ds_read_b96 v[32:34], v6
	ds_read_b96 v[36:38], v6 offset:16
	ds_read_b96 v[40:42], v6 offset:32
	ds_read_b96 v[44:46], v6 offset:48
	ds_read2_b32 v[48:49], v3 offset0:0 offset1:1
	ds_read_b32 v56, v3 offset:8
	ds_read2_b32 v[50:51], v3 offset0:192 offset1:193
	ds_read_b32 v57, v3 offset:776
	ds_read2_b32 v[52:53], v4 offset0:0 offset1:1
	ds_read_b32 v58, v4 offset:8
	ds_read2_b32 v[54:55], v4 offset0:192 offset1:193
	ds_read_b32 v59, v4 offset:776
	s_waitcnt lgkmcnt(6)
	v_fma_f32 v60, v48, v32, v44
	v_fma_f32 v61, v48, v33, v45
	v_fma_f32 v62, v48, v34, v46
	v_fmac_f32_e32 v60, v49, v36
	v_fmac_f32_e32 v61, v49, v37
	v_fmac_f32_e32 v62, v49, v38
	v_fmac_f32_e32 v60, v56, v40
	v_fmac_f32_e32 v61, v56, v41
	v_fmac_f32_e32 v62, v56, v42
	ds_write2_b32 v3, v60, v61 offset0:0 offset1:1
	ds_write_b32 v3, v62 offset:8
	s_waitcnt lgkmcnt(6)
	v_fma_f32 v35, v50, v32, v44
	v_fma_f32 v39, v50, v33, v45
	v_fma_f32 v43, v50, v34, v46
	v_fmac_f32_e32 v35, v51, v36
	v_fmac_f32_e32 v39, v51, v37
	v_fmac_f32_e32 v43, v51, v38
	v_fmac_f32_e32 v35, v57, v40
	v_fmac_f32_e32 v39, v57, v41
	v_fmac_f32_e32 v43, v57, v42
	ds_write2_b32 v3, v35, v39 offset0:192 offset1:193
	ds_write_b32 v3, v43 offset:776
	s_waitcnt lgkmcnt(6)
	v_fma_f32 v60, v52, v32, v44
	v_fma_f32 v61, v52, v33, v45
	v_fma_f32 v62, v52, v34, v46
	v_fmac_f32_e32 v60, v53, v36
	v_fmac_f32_e32 v61, v53, v37
	v_fmac_f32_e32 v62, v53, v38
	v_fmac_f32_e32 v60, v58, v40
	v_fmac_f32_e32 v61, v58, v41
	v_fmac_f32_e32 v62, v58, v42
	ds_write2_b32 v4, v60, v61 offset0:0 offset1:1
	ds_write_b32 v4, v62 offset:8
	s_waitcnt lgkmcnt(6)
	v_fma_f32 v35, v54, v32, v44
	v_fma_f32 v39, v54, v33, v45
	v_fma_f32 v43, v54, v34, v46
	v_fmac_f32_e32 v35, v55, v36
	v_fmac_f32_e32 v39, v55, v37
	v_fmac_f32_e32 v43, v55, v38
	v_fmac_f32_e32 v35, v59, v40
	v_fmac_f32_e32 v39, v59, v41
	v_fmac_f32_e32 v43, v59, v42
	ds_write2_b32 v4, v35, v39 offset0:192 offset1:193
	ds_write_b32 v4, v43 offset:776
	ds_read_b128 v[8:11], v2
	ds_read_b128 v[12:15], v2 offset:1024
	ds_read_b128 v[16:19], v2 offset:2048
	s_waitcnt lgkmcnt(2)
	global_store_dwordx4 v1, v[8:11], s[10:11] offset:-2048 nt
	s_waitcnt lgkmcnt(1)
	global_store_dwordx4 v1, v[12:15], s[10:11] offset:-1024 nt
	s_waitcnt lgkmcnt(0)
	global_store_dwordx4 v1, v[16:19], s[10:11] offset:0 nt
	s_waitcnt vmcnt(3)
	ds_write_b128 v2, v[20:23]
	ds_write_b128 v2, v[24:27] offset:1024
	ds_write_b128 v2, v[28:31] offset:2048
	ds_read2_b32 v[48:49], v3 offset0:0 offset1:1
	ds_read_b32 v56, v3 offset:8
	ds_read2_b32 v[50:51], v3 offset0:192 offset1:193
	ds_read_b32 v57, v3 offset:776
	ds_read2_b32 v[52:53], v4 offset0:0 offset1:1
	ds_read_b32 v58, v4 offset:8
	ds_read2_b32 v[54:55], v4 offset0:192 offset1:193
	ds_read_b32 v59, v4 offset:776
	s_waitcnt lgkmcnt(6)
	v_fma_f32 v60, v48, v32, v44
	v_fma_f32 v61, v48, v33, v45
	v_fma_f32 v62, v48, v34, v46
	v_fmac_f32_e32 v60, v49, v36
	v_fmac_f32_e32 v61, v49, v37
	v_fmac_f32_e32 v62, v49, v38
	v_fmac_f32_e32 v60, v56, v40
	v_fmac_f32_e32 v61, v56, v41
	v_fmac_f32_e32 v62, v56, v42
	ds_write2_b32 v3, v60, v61 offset0:0 offset1:1
	ds_write_b32 v3, v62 offset:8
	s_waitcnt lgkmcnt(6)
	v_fma_f32 v35, v50, v32, v44
	v_fma_f32 v39, v50, v33, v45
	v_fma_f32 v43, v50, v34, v46
	v_fmac_f32_e32 v35, v51, v36
	v_fmac_f32_e32 v39, v51, v37
	v_fmac_f32_e32 v43, v51, v38
	v_fmac_f32_e32 v35, v57, v40
	v_fmac_f32_e32 v39, v57, v41
	v_fmac_f32_e32 v43, v57, v42
	ds_write2_b32 v3, v35, v39 offset0:192 offset1:193
	ds_write_b32 v3, v43 offset:776
	s_waitcnt lgkmcnt(6)
	v_fma_f32 v60, v52, v32, v44
	v_fma_f32 v61, v52, v33, v45
	v_fma_f32 v62, v52, v34, v46
	v_fmac_f32_e32 v60, v53, v36
	v_fmac_f32_e32 v61, v53, v37
	v_fmac_f32_e32 v62, v53, v38
	v_fmac_f32_e32 v60, v58, v40
	v_fmac_f32_e32 v61, v58, v41
	v_fmac_f32_e32 v62, v58, v42
	ds_write2_b32 v4, v60, v61 offset0:0 offset1:1
	ds_write_b32 v4, v62 offset:8
	s_waitcnt lgkmcnt(6)
	v_fma_f32 v35, v54, v32, v44
	v_fma_f32 v39, v54, v33, v45
	v_fma_f32 v43, v54, v34, v46
	v_fmac_f32_e32 v35, v55, v36
	v_fmac_f32_e32 v39, v55, v37
	v_fmac_f32_e32 v43, v55, v38
	v_fmac_f32_e32 v35, v59, v40
	v_fmac_f32_e32 v39, v59, v41
	v_fmac_f32_e32 v43, v59, v42
	ds_write2_b32 v4, v35, v39 offset0:192 offset1:193
	ds_write_b32 v4, v43 offset:776
	ds_read_b128 v[20:23], v2
	ds_read_b128 v[24:27], v2 offset:1024
	ds_read_b128 v[28:31], v2 offset:2048
	s_waitcnt lgkmcnt(2)
	global_store_dwordx4 v1, v[20:23], s[10:11] offset:1024 nt
	s_waitcnt lgkmcnt(1)
	global_store_dwordx4 v1, v[24:27], s[10:11] offset:2048 nt
	s_waitcnt lgkmcnt(0)
	s_and_saveexec_b64 s[16:17], s[14:15]
	global_store_dwordx4 v1, v[28:31], s[10:11] offset:3072 nt
	s_endpgm
